# speedup vs baseline: 1.0614x; 1.0304x over previous
.Lpro_zero:
	v_add_u32_e32 v78, 64, v78
	v_cmp_lt_u32_e32 vcc, s3, v78
	ds_write_b128 v79, v[74:77]
	s_or_b64 s[0:1], vcc, s[0:1]
	v_add_u32_e32 v79, 0x400, v79
	s_andn2_b64 exec, exec, s[0:1]
	s_cbranch_execnz .Lpro_zero
	s_or_b64 exec, exec, s[0:1]
	v_mov_b32_e32 v3, 0x3c00
	v_cndmask_b32_e64 v3, 0, v3, s[4:5]
	v_pack_b32_f16 v96, v3, 0
	v_mov_b32_e32 v97, 0
	v_mov_b32_e32 v98, 0
	v_mov_b32_e32 v99, 0
	v_mov_b32_e32 v77, 0
	v_mov_b32_e32 v78, 0
	v_mov_b32_e32 v79, 0
	v_mov_b32_e32 v53, 0
	v_mov_b32_e32 v54, 0
	v_mov_b32_e32 v55, 0
	s_waitcnt vmcnt(43)
	v_and_b32_e32 v76, 0xffff, v72
	v_and_b32_e32 v52, 0xffff, v73
	s_nop 1
	v_mfma_f32_32x32x16_f16 v[2:17], v[76:79], v[96:99], 0
	v_mfma_f32_32x32x16_f16 v[18:33], v[52:55], v[96:99], 0
	s_waitcnt vmcnt(31)
	v_mfma_f32_32x32x16_f16 v[2:17], v[220:223], v[56:59], v[2:17]
	v_mfma_f32_32x32x16_f16 v[18:33], v[224:227], v[56:59], v[18:33]
	v_mfma_f32_32x32x16_f16 v[2:17], v[228:231], v[60:63], v[2:17]
	v_mfma_f32_32x32x16_f16 v[18:33], v[232:235], v[60:63], v[18:33]
	v_mfma_f32_32x32x16_f16 v[2:17], v[236:239], v[64:67], v[2:17]
	v_mfma_f32_32x32x16_f16 v[18:33], v[240:243], v[64:67], v[18:33]
	v_mfma_f32_32x32x16_f16 v[2:17], v[244:247], v[68:71], v[2:17]
	v_mfma_f32_32x32x16_f16 v[18:33], v[248:251], v[68:71], v[18:33]
	v_readfirstlane_b32 s0, v0
	s_mov_b32 s3, 0
	s_nop 11
	v_cvt_pk_f16_f32 v9, v8, v9
	v_cvt_pk_f16_f32 v8, v6, v7
	v_cvt_pk_f16_f32 v7, v4, v5
	v_cvt_pk_f16_f32 v6, v2, v3
	v_cvt_pk_f16_f32 v5, v24, v25
	v_cvt_pk_f16_f32 v4, v22, v23
	v_cvt_pk_f16_f32 v3, v20, v21
	v_cvt_pk_f16_f32 v2, v18, v19
	v_cvt_pk_f16_f32 v17, v16, v17
	v_cvt_pk_f16_f32 v16, v14, v15
	v_cvt_pk_f16_f32 v15, v12, v13
	v_cvt_pk_f16_f32 v14, v10, v11
	v_cvt_pk_f16_f32 v11, v32, v33
	v_cvt_pk_f16_f32 v10, v30, v31
	v_lshlrev_b32_e32 v34, 7, v212
	v_lshl_add_u32 v34, v51, 3, v34
	s_movk_i32 s8, 0x3540
	v_add3_u32 v34, v34, v50, s8
	ds_write2_b64 v34, v[6:7], v[8:9] offset1:2
	ds_write2_b64 v34, v[14:15], v[16:17] offset0:4 offset1:6
	ds_write2_b64 v34, v[2:3], v[4:5] offset0:8 offset1:10
	v_cvt_pk_f16_f32 v9, v28, v29
	v_cvt_pk_f16_f32 v8, v26, v27
	ds_write2_b64 v34, v[8:9], v[10:11] offset0:12 offset1:14
	s_cmpk_lt_i32 s0, 0x100
	s_cselect_b32 s44, 0, 1
.LBB0_20:
	v_mov_b32_e32 v81, 0
	v_lshlrev_b32_e32 v4, 3, v0
	v_lshrrev_b32_e32 v2, 2, v0
	v_lshlrev_b32_e32 v3, 1, v0
	v_bfe_i32 v5, v0, 0, 1
	v_lshrrev_b32_e32 v0, 5, v0
	v_and_b32_e32 v5, 0x120, v5
	v_and_b32_e32 v221, 12, v0
	v_add_u16_e32 v0, v214, v212
	v_add_u32_e32 v5, v50, v5
	v_mul_u32_u24_e32 v1, 0x2800, v1
	v_lshrrev_b16_e32 v0, 1, v0
	v_or_b32_e32 v1, v1, v214
	v_lshl_add_u32 v223, v0, 2, v5
	v_add_lshl_u32 v0, v214, v212, 1
	v_lshlrev_b32_e32 v216, 2, v51
	s_movk_i32 s0, 0x88
	v_add_u32_e32 v222, 0x22a00, v1
	v_add_u32_e32 v1, 64, v0
	v_add_u32_e32 v0, 0xc0, v0
	v_and_or_b32 v2, v2, 3, v216
	v_lshlrev_b32_e32 v6, 4, v212
	v_mad_u32_u24 v8, v212, s0, v50
	v_and_b32_e32 v0, 0x1fc, v0
	s_movk_i32 s0, 0x880
	v_mul_u32_u24_e32 v2, 0x88, v2
	v_and_b32_e32 v3, 32, v3
	v_add_u32_e32 v7, v50, v6
	v_add_u32_e32 v225, v5, v0
	v_mad_u32_u24 v0, v51, s0, v50
	s_movk_i32 s0, 0x240
	v_and_b32_e32 v4, 24, v4
	v_add3_u32 v2, v50, v2, v3
	v_and_b32_e32 v1, 0xfc, v1
	v_add3_u32 v226, v0, v6, s0
	v_add_u32_e32 v228, v7, v214
	v_mbcnt_lo_u32_b32 v0, -1, 0
	v_and_b32_e32 v80, 0xffff, v39
	v_mov_b32_e32 v82, v81
	v_mov_b32_e32 v83, v81
	v_and_b32_e32 v204, 0xffff, v38
	v_mov_b32_e32 v205, v81
	v_mov_b32_e32 v206, v81
	v_mov_b32_e32 v207, v81
	v_lshl_add_u32 v220, v215, 1, v50
	v_add_u32_e32 v224, v5, v1
	s_brev_b32 s33, 61
	s_brev_b32 s34, 60
	s_mov_b32 s35, 0x7fff7fff
	s_mov_b32 s42, 0xa714a714
	v_mov_b32_e32 v227, 0xb7d0b7d0
	s_mov_b32 s43, 0xbc90bc90
	v_add_u32_e32 v229, v8, v214
	v_add_u32_e32 v230, v2, v4
	v_add_u32_e32 v231, 0xf0, v228
	v_add_u32_e32 v232, 0x170, v228
	v_add_u32_e32 v233, 0x1f0, v228
	v_add_u32_e32 v234, 0x70, v228
	v_mbcnt_hi_u32_b32 v235, -1, v0
	v_add_u32_e32 v246, 0x2000, v229
	v_xor_b32_e32 v245, 32, v235
	v_lshlrev_b32_e32 v245, 2, v245
	v_and_b32_e32 v247, 15, v215
	v_lshrrev_b32_e32 v248, 4, v215
	s_movk_i32 s0, 0x2440
	v_mul_u32_u24_e32 v249, 0x88, v247
	v_lshl_add_u32 v249, v248, 4, v249
	v_add3_u32 v249, v249, v50, s0
	v_add_u32_e32 v250, 0x880, v249
	v_bfe_u32 v251, v215, 2, 2
	v_lshl_add_u32 v251, v248, 2, v251
	v_mul_u32_u24_e32 v251, 0x88, v251
	v_and_b32_e32 v252, 3, v215
	v_lshl_add_u32 v251, v252, 3, v251
	v_add3_u32 v251, v251, v50, s0
	v_sub_u32_e32 v252, v222, v214
	v_lshl_add_u32 v252, v248, 3, v252
	v_lshlrev_b32_e32 v253, 7, v247
	v_lshl_add_u32 v253, v248, 4, v253
	s_movk_i32 s0, 0x3540
	v_add3_u32 v248, v253, v50, s0
	v_xor_b32_e32 v247, 16, v215
	v_lshlrev_b32_e32 v247, 2, v247
	s_waitcnt vmcnt(28)
	s_branch .LBB0_22

.Lprio_done:
	s_cmp_eq_u32 s3, 3
	v_lshl_add_u32 v0, s3, 17, v217
	v_add_u32_e32 v1, 0x20000, v0
	s_cselect_b64 vcc, -1, 0
	v_cndmask_b32_e32 v0, v1, v0, vcc
	v_or_b32_e32 v0, v0, v215
	v_ashrrev_i32_e32 v1, 31, v0
	v_lshl_add_u64 v[0:1], v[0:1], 2, s[40:41]
	v_mov_b32_e32 v2, v219
	v_mov_b32_e32 v3, v218
	global_load_dword v218, v[0:1], off
	global_load_dword v219, v[0:1], off offset:256
	v_add_f32_e32 v0, v2, v3
	s_nop 1
	v_add_f32_dpp v0, v0, v0 quad_perm:[1,0,3,2] row_mask:0xf bank_mask:0xf bound_ctrl:1
	s_nop 1
	v_add_f32_dpp v0, v0, v0 quad_perm:[2,3,0,1] row_mask:0xf bank_mask:0xf bound_ctrl:1
	s_nop 1
	v_add_f32_dpp v0, v0, v0 row_half_mirror row_mask:0xf bank_mask:0xf bound_ctrl:1
	s_nop 1
	v_add_f32_dpp v0, v0, v0 row_mirror row_mask:0xf bank_mask:0xf bound_ctrl:1
	s_nop 0
	v_readlane_b32 s1, v0, 16
	v_readlane_b32 s9, v0, 48
	v_readlane_b32 s0, v0, 0
	v_readlane_b32 s8, v0, 32
	v_mov_b32_e32 v0, s1
	v_mov_b32_e32 v1, s9
	v_add_f32_e32 v0, s0, v0
	v_add_f32_e32 v1, s8, v1
	v_add_f32_e32 v0, v0, v1
	v_fma_mixlo_f16 v1, v0, s33, v3
	v_fma_mixlo_f16 v0, v0, s33, v2
	ds_write_b16 v220, v1 offset:14
	ds_write_b16 v220, v0 offset:142
	ds_write_b16 v220, v1 offset:300
	ds_write_b16 v220, v0 offset:428
	ds_read2_b32 v[2:3], v223 offset0:2 offset1:3
	ds_read2_b32 v[0:1], v223 offset1:1
	ds_read2_b32 v[4:5], v223 offset0:32 offset1:33
	ds_read2_b32 v[6:7], v223 offset0:34 offset1:35
	s_mov_b32 s8, 0
	s_mov_b32 s9, s8
	s_mov_b32 s10, s8
	s_waitcnt lgkmcnt(3)
	v_or_b32_sdwa v8, v3, s34 dst_sel:DWORD dst_unused:UNUSED_PAD src0_sel:WORD_0 src1_sel:DWORD
	v_cndmask_b32_e64 v3, v8, v3, s[4:5]
	s_mov_b32 s11, s8
	s_mov_b32 s12, s8
	s_waitcnt lgkmcnt(2)
	v_mfma_f32_32x32x16_f16 v[64:79], v[200:203], v[0:3], 0
	ds_read2_b32 v[2:3], v224 offset0:2 offset1:3
	ds_read2_b32 v[0:1], v224 offset1:1
	ds_read2_b32 v[16:17], v225 offset1:1
	ds_read2_b32 v[18:19], v225 offset0:2 offset1:3
	s_mov_b32 s13, s8
	s_mov_b32 s14, s8
	s_mov_b32 s15, s8
	s_waitcnt lgkmcnt(3)
	v_or_b32_sdwa v8, v3, s34 dst_sel:DWORD dst_unused:UNUSED_PAD src0_sel:WORD_0 src1_sel:DWORD
	s_waitcnt lgkmcnt(0)
	v_or_b32_sdwa v20, v19, s34 dst_sel:DWORD dst_unused:UNUSED_PAD src0_sel:WORD_0 src1_sel:DWORD
	v_cndmask_b32_e64 v19, v20, v19, s[4:5]
	v_cndmask_b32_e64 v3, v8, v3, s[4:5]
	s_mov_b32 s16, s8
	v_mfma_f32_32x32x16_f16 v[16:31], v[200:203], v[16:19], 0
	s_mov_b32 s17, s8
	s_mov_b32 s18, s8
	s_mov_b32 s19, s8
	s_mov_b32 s20, s8
	s_mov_b32 s21, s8
	s_mov_b32 s22, s8
	s_mov_b32 s23, s8
	v_mfma_f32_32x32x16_f16 v[48:63], v[200:203], v[0:3], 0
	v_or_b32_sdwa v0, v7, s34 dst_sel:DWORD dst_unused:UNUSED_PAD src0_sel:WORD_0 src1_sel:DWORD
	v_cndmask_b32_e64 v7, v0, v7, s[4:5]
	s_nop 1
	v_mfma_f32_32x32x16_f16 v[32:47], v[200:203], v[4:7], 0
	v_mov_b64_e32 v[0:1], s[8:9]
	v_mov_b64_e32 v[2:3], s[10:11]
	v_mov_b64_e32 v[4:5], s[12:13]
	v_mov_b64_e32 v[6:7], s[14:15]
	v_mov_b64_e32 v[8:9], s[16:17]
	v_mov_b64_e32 v[10:11], s[18:19]
	v_mov_b64_e32 v[12:13], s[20:21]
	v_mov_b64_e32 v[14:15], s[22:23]
	s_nop 15
	s_nop 3
	v_cvt_pk_f16_f32 v239, v64, v65
	v_cvt_pk_f16_f32 v240, v66, v67
	v_and_b32 v209, s35, v239
	v_and_b32 v238, s35, v240
	v_pk_fma_f16 v236, v209, s42, v227
	v_pk_fma_f16 v237, v238, s42, v227
	v_pk_fma_f16 v236, v236, v209, s43
	v_pk_fma_f16 v237, v237, v238, s43
	s_nop 0
	v_pk_mul_f16 v236, v236, v209
	v_pk_mul_f16 v237, v237, v238
	v_exp_f16_sdwa v236, v236 dst_sel:WORD_0 dst_unused:UNUSED_PRESERVE src0_sel:WORD_0
	v_exp_f16_sdwa v237, v237 dst_sel:WORD_0 dst_unused:UNUSED_PRESERVE src0_sel:WORD_0
	v_exp_f16_sdwa v236, v236 dst_sel:WORD_1 dst_unused:UNUSED_PRESERVE src0_sel:WORD_1
	v_exp_f16_sdwa v237, v237 dst_sel:WORD_1 dst_unused:UNUSED_PRESERVE src0_sel:WORD_1
	v_pk_add_f16 v64, v239, v209
	v_pk_add_f16 v65, v240, v238
	v_pk_fma_f16 v236, v209, v236, v64 neg_lo:[1,0,0] neg_hi:[1,0,0]
	v_pk_fma_f16 v237, v238, v237, v65 neg_lo:[1,0,0] neg_hi:[1,0,0]
	s_nop 0
	v_cvt_pk_f16_f32 v209, v68, v69
	v_cvt_pk_f16_f32 v238, v70, v71
	v_and_b32 v66, s35, v209
	v_and_b32 v67, s35, v238
	v_pk_fma_f16 v64, v66, s42, v227
	v_pk_fma_f16 v65, v67, s42, v227
	v_pk_fma_f16 v64, v64, v66, s43
	v_pk_fma_f16 v65, v65, v67, s43
	s_nop 0
	v_pk_mul_f16 v64, v64, v66
	v_pk_mul_f16 v65, v65, v67
	v_exp_f16_sdwa v64, v64 dst_sel:WORD_0 dst_unused:UNUSED_PRESERVE src0_sel:WORD_0
	v_exp_f16_sdwa v65, v65 dst_sel:WORD_0 dst_unused:UNUSED_PRESERVE src0_sel:WORD_0
	v_exp_f16_sdwa v64, v64 dst_sel:WORD_1 dst_unused:UNUSED_PRESERVE src0_sel:WORD_1
	v_exp_f16_sdwa v65, v65 dst_sel:WORD_1 dst_unused:UNUSED_PRESERVE src0_sel:WORD_1
	v_pk_add_f16 v68, v209, v66
	v_pk_add_f16 v69, v238, v67
	v_pk_fma_f16 v64, v66, v64, v68 neg_lo:[1,0,0] neg_hi:[1,0,0]
	v_pk_fma_f16 v65, v67, v65, v69 neg_lo:[1,0,0] neg_hi:[1,0,0]
	s_nop 0
	v_cvt_pk_f16_f32 v70, v72, v73
	v_cvt_pk_f16_f32 v71, v74, v75
	v_and_b32 v68, s35, v70
	v_and_b32 v69, s35, v71
	v_pk_fma_f16 v66, v68, s42, v227
	v_pk_fma_f16 v67, v69, s42, v227
	v_pk_fma_f16 v66, v66, v68, s43
	v_pk_fma_f16 v67, v67, v69, s43
	s_nop 0
	v_pk_mul_f16 v66, v66, v68
	v_pk_mul_f16 v67, v67, v69
	v_exp_f16_sdwa v66, v66 dst_sel:WORD_0 dst_unused:UNUSED_PRESERVE src0_sel:WORD_0
	v_exp_f16_sdwa v67, v67 dst_sel:WORD_0 dst_unused:UNUSED_PRESERVE src0_sel:WORD_0
	v_exp_f16_sdwa v66, v66 dst_sel:WORD_1 dst_unused:UNUSED_PRESERVE src0_sel:WORD_1
	v_exp_f16_sdwa v67, v67 dst_sel:WORD_1 dst_unused:UNUSED_PRESERVE src0_sel:WORD_1
	v_pk_add_f16 v72, v70, v68
	v_pk_add_f16 v73, v71, v69
	v_pk_fma_f16 v66, v68, v66, v72 neg_lo:[1,0,0] neg_hi:[1,0,0]
	v_pk_fma_f16 v67, v69, v67, v73 neg_lo:[1,0,0] neg_hi:[1,0,0]
	s_nop 0
	v_cvt_pk_f16_f32 v72, v76, v77
	v_cvt_pk_f16_f32 v73, v78, v79
	v_and_b32 v70, s35, v72
	v_and_b32 v71, s35, v73
	v_pk_fma_f16 v68, v70, s42, v227
	v_pk_fma_f16 v69, v71, s42, v227
	v_pk_fma_f16 v68, v68, v70, s43
	v_pk_fma_f16 v69, v69, v71, s43
	s_nop 0
	v_pk_mul_f16 v68, v68, v70
	v_pk_mul_f16 v69, v69, v71
	v_exp_f16_sdwa v68, v68 dst_sel:WORD_0 dst_unused:UNUSED_PRESERVE src0_sel:WORD_0
	v_exp_f16_sdwa v69, v69 dst_sel:WORD_0 dst_unused:UNUSED_PRESERVE src0_sel:WORD_0
	v_exp_f16_sdwa v68, v68 dst_sel:WORD_1 dst_unused:UNUSED_PRESERVE src0_sel:WORD_1
	v_exp_f16_sdwa v69, v69 dst_sel:WORD_1 dst_unused:UNUSED_PRESERVE src0_sel:WORD_1
	v_pk_add_f16 v74, v72, v70
	v_pk_add_f16 v75, v73, v71
	v_pk_fma_f16 v68, v70, v68, v74 neg_lo:[1,0,0] neg_hi:[1,0,0]
	v_pk_fma_f16 v69, v71, v69, v75 neg_lo:[1,0,0] neg_hi:[1,0,0]
	s_nop 0
	v_cvt_pk_f16_f32 v74, v48, v49
	v_cvt_pk_f16_f32 v75, v50, v51
	v_and_b32 v72, s35, v74
	v_and_b32 v73, s35, v75
	v_pk_fma_f16 v70, v72, s42, v227
	v_pk_fma_f16 v71, v73, s42, v227
	v_pk_fma_f16 v70, v70, v72, s43
	v_pk_fma_f16 v71, v71, v73, s43
	s_nop 0
	v_pk_mul_f16 v70, v70, v72
	v_pk_mul_f16 v71, v71, v73
	v_exp_f16_sdwa v70, v70 dst_sel:WORD_0 dst_unused:UNUSED_PRESERVE src0_sel:WORD_0
	v_exp_f16_sdwa v71, v71 dst_sel:WORD_0 dst_unused:UNUSED_PRESERVE src0_sel:WORD_0
	v_exp_f16_sdwa v70, v70 dst_sel:WORD_1 dst_unused:UNUSED_PRESERVE src0_sel:WORD_1
	v_exp_f16_sdwa v71, v71 dst_sel:WORD_1 dst_unused:UNUSED_PRESERVE src0_sel:WORD_1
	v_pk_add_f16 v48, v74, v72
	v_pk_add_f16 v49, v75, v73
	v_pk_fma_f16 v70, v72, v70, v48 neg_lo:[1,0,0] neg_hi:[1,0,0]
	v_pk_fma_f16 v71, v73, v71, v49 neg_lo:[1,0,0] neg_hi:[1,0,0]
	s_nop 0
	v_cvt_pk_f16_f32 v72, v52, v53
	v_cvt_pk_f16_f32 v73, v54, v55
	v_and_b32 v50, s35, v72
	v_and_b32 v51, s35, v73
	v_pk_fma_f16 v48, v50, s42, v227
	v_pk_fma_f16 v49, v51, s42, v227
	v_pk_fma_f16 v48, v48, v50, s43
	v_pk_fma_f16 v49, v49, v51, s43
	s_nop 0
	v_pk_mul_f16 v48, v48, v50
	v_pk_mul_f16 v49, v49, v51
	v_exp_f16_sdwa v48, v48 dst_sel:WORD_0 dst_unused:UNUSED_PRESERVE src0_sel:WORD_0
	v_exp_f16_sdwa v49, v49 dst_sel:WORD_0 dst_unused:UNUSED_PRESERVE src0_sel:WORD_0
	v_exp_f16_sdwa v48, v48 dst_sel:WORD_1 dst_unused:UNUSED_PRESERVE src0_sel:WORD_1
	v_exp_f16_sdwa v49, v49 dst_sel:WORD_1 dst_unused:UNUSED_PRESERVE src0_sel:WORD_1
	v_pk_add_f16 v52, v72, v50
	v_pk_add_f16 v53, v73, v51
	v_pk_fma_f16 v48, v50, v48, v52 neg_lo:[1,0,0] neg_hi:[1,0,0]
	v_pk_fma_f16 v49, v51, v49, v53 neg_lo:[1,0,0] neg_hi:[1,0,0]
	s_nop 0
	v_cvt_pk_f16_f32 v54, v56, v57
	v_cvt_pk_f16_f32 v55, v58, v59
	v_and_b32 v52, s35, v54
	v_and_b32 v53, s35, v55
	v_pk_fma_f16 v50, v52, s42, v227
	v_pk_fma_f16 v51, v53, s42, v227
	v_pk_fma_f16 v50, v50, v52, s43
	v_pk_fma_f16 v51, v51, v53, s43
	s_nop 0
	v_pk_mul_f16 v50, v50, v52
	v_pk_mul_f16 v51, v51, v53
	v_exp_f16_sdwa v50, v50 dst_sel:WORD_0 dst_unused:UNUSED_PRESERVE src0_sel:WORD_0
	v_exp_f16_sdwa v51, v51 dst_sel:WORD_0 dst_unused:UNUSED_PRESERVE src0_sel:WORD_0
	v_exp_f16_sdwa v50, v50 dst_sel:WORD_1 dst_unused:UNUSED_PRESERVE src0_sel:WORD_1
	v_exp_f16_sdwa v51, v51 dst_sel:WORD_1 dst_unused:UNUSED_PRESERVE src0_sel:WORD_1
	v_pk_add_f16 v56, v54, v52
	v_pk_add_f16 v57, v55, v53
	v_pk_fma_f16 v50, v52, v50, v56 neg_lo:[1,0,0] neg_hi:[1,0,0]
	v_pk_fma_f16 v51, v53, v51, v57 neg_lo:[1,0,0] neg_hi:[1,0,0]
	s_nop 0
	v_cvt_pk_f16_f32 v56, v60, v61
	v_cvt_pk_f16_f32 v57, v62, v63
	v_and_b32 v54, s35, v56
	v_and_b32 v55, s35, v57
	v_pk_fma_f16 v52, v54, s42, v227
	v_pk_fma_f16 v53, v55, s42, v227
	v_pk_fma_f16 v52, v52, v54, s43
	v_pk_fma_f16 v53, v53, v55, s43
	s_nop 0
	v_pk_mul_f16 v52, v52, v54
	v_pk_mul_f16 v53, v53, v55
	v_exp_f16_sdwa v52, v52 dst_sel:WORD_0 dst_unused:UNUSED_PRESERVE src0_sel:WORD_0
	v_exp_f16_sdwa v53, v53 dst_sel:WORD_0 dst_unused:UNUSED_PRESERVE src0_sel:WORD_0
	v_exp_f16_sdwa v52, v52 dst_sel:WORD_1 dst_unused:UNUSED_PRESERVE src0_sel:WORD_1
	v_exp_f16_sdwa v53, v53 dst_sel:WORD_1 dst_unused:UNUSED_PRESERVE src0_sel:WORD_1
	v_pk_add_f16 v58, v56, v54
	v_pk_add_f16 v59, v57, v55
	v_pk_fma_f16 v52, v54, v52, v58 neg_lo:[1,0,0] neg_hi:[1,0,0]
	v_pk_fma_f16 v53, v55, v53, v59 neg_lo:[1,0,0] neg_hi:[1,0,0]
	ds_write2_b64 v228, v[236:237], v[70:71] offset0:78 offset1:142
	ds_write2st64_b64 v231, v[64:65], v[48:49] offset0:5 offset1:6
	ds_write2st64_b64 v232, v[66:67], v[50:51] offset0:9 offset1:10
	ds_write2st64_b64 v233, v[68:69], v[52:53] offset0:13 offset1:14
	v_cvt_pk_f16_f32 v52, v32, v33
	v_cvt_pk_f16_f32 v53, v34, v35
	v_and_b32 v50, s35, v52
	v_and_b32 v51, s35, v53
	v_pk_fma_f16 v48, v50, s42, v227
	v_pk_fma_f16 v49, v51, s42, v227
	v_pk_fma_f16 v48, v48, v50, s43
	v_pk_fma_f16 v49, v49, v51, s43
	v_mov_b32_e32 v237, 0xff800000
	v_pk_mul_f16 v48, v48, v50
	v_pk_mul_f16 v49, v49, v51
	v_exp_f16_sdwa v48, v48 dst_sel:WORD_0 dst_unused:UNUSED_PRESERVE src0_sel:WORD_0
	v_exp_f16_sdwa v49, v49 dst_sel:WORD_0 dst_unused:UNUSED_PRESERVE src0_sel:WORD_0
	v_exp_f16_sdwa v48, v48 dst_sel:WORD_1 dst_unused:UNUSED_PRESERVE src0_sel:WORD_1
	v_exp_f16_sdwa v49, v49 dst_sel:WORD_1 dst_unused:UNUSED_PRESERVE src0_sel:WORD_1
	v_pk_add_f16 v32, v52, v50
	v_pk_add_f16 v33, v53, v51
	v_pk_fma_f16 v48, v50, v48, v32 neg_lo:[1,0,0] neg_hi:[1,0,0]
	v_pk_fma_f16 v49, v51, v49, v33 neg_lo:[1,0,0] neg_hi:[1,0,0]
	v_mov_b32_e32 v236, 0
	v_cvt_pk_f16_f32 v50, v36, v37
	v_cvt_pk_f16_f32 v51, v38, v39
	v_and_b32 v34, s35, v50
	v_and_b32 v35, s35, v51
	v_pk_fma_f16 v32, v34, s42, v227
	v_pk_fma_f16 v33, v35, s42, v227
	v_pk_fma_f16 v32, v32, v34, s43
	v_pk_fma_f16 v33, v33, v35, s43
	s_nop 0
	v_pk_mul_f16 v32, v32, v34
	v_pk_mul_f16 v33, v33, v35
	v_exp_f16_sdwa v32, v32 dst_sel:WORD_0 dst_unused:UNUSED_PRESERVE src0_sel:WORD_0
	v_exp_f16_sdwa v33, v33 dst_sel:WORD_0 dst_unused:UNUSED_PRESERVE src0_sel:WORD_0
	v_exp_f16_sdwa v32, v32 dst_sel:WORD_1 dst_unused:UNUSED_PRESERVE src0_sel:WORD_1
	v_exp_f16_sdwa v33, v33 dst_sel:WORD_1 dst_unused:UNUSED_PRESERVE src0_sel:WORD_1
	v_pk_add_f16 v36, v50, v34
	v_pk_add_f16 v37, v51, v35
	v_pk_fma_f16 v32, v34, v32, v36 neg_lo:[1,0,0] neg_hi:[1,0,0]
	v_pk_fma_f16 v33, v35, v33, v37 neg_lo:[1,0,0] neg_hi:[1,0,0]
	s_nop 0
	v_cvt_pk_f16_f32 v38, v40, v41
	v_cvt_pk_f16_f32 v39, v42, v43
	v_and_b32 v36, s35, v38
	v_and_b32 v37, s35, v39
	v_pk_fma_f16 v34, v36, s42, v227
	v_pk_fma_f16 v35, v37, s42, v227
	v_pk_fma_f16 v34, v34, v36, s43
	v_pk_fma_f16 v35, v35, v37, s43
	s_nop 0
	v_pk_mul_f16 v34, v34, v36
	v_pk_mul_f16 v35, v35, v37
	v_exp_f16_sdwa v34, v34 dst_sel:WORD_0 dst_unused:UNUSED_PRESERVE src0_sel:WORD_0
	v_exp_f16_sdwa v35, v35 dst_sel:WORD_0 dst_unused:UNUSED_PRESERVE src0_sel:WORD_0
	v_exp_f16_sdwa v34, v34 dst_sel:WORD_1 dst_unused:UNUSED_PRESERVE src0_sel:WORD_1
	v_exp_f16_sdwa v35, v35 dst_sel:WORD_1 dst_unused:UNUSED_PRESERVE src0_sel:WORD_1
	v_pk_add_f16 v40, v38, v36
	v_pk_add_f16 v41, v39, v37
	v_pk_fma_f16 v34, v36, v34, v40 neg_lo:[1,0,0] neg_hi:[1,0,0]
	v_pk_fma_f16 v35, v37, v35, v41 neg_lo:[1,0,0] neg_hi:[1,0,0]
	s_nop 0
	v_cvt_pk_f16_f32 v40, v44, v45
	v_cvt_pk_f16_f32 v41, v46, v47
	v_and_b32 v38, s35, v40
	v_and_b32 v39, s35, v41
	v_pk_fma_f16 v36, v38, s42, v227
	v_pk_fma_f16 v37, v39, s42, v227
	v_pk_fma_f16 v36, v36, v38, s43
	v_pk_fma_f16 v37, v37, v39, s43
	s_nop 0
	v_pk_mul_f16 v36, v36, v38
	v_pk_mul_f16 v37, v37, v39
	v_exp_f16_sdwa v36, v36 dst_sel:WORD_0 dst_unused:UNUSED_PRESERVE src0_sel:WORD_0
	v_exp_f16_sdwa v37, v37 dst_sel:WORD_0 dst_unused:UNUSED_PRESERVE src0_sel:WORD_0
	v_exp_f16_sdwa v36, v36 dst_sel:WORD_1 dst_unused:UNUSED_PRESERVE src0_sel:WORD_1
	v_exp_f16_sdwa v37, v37 dst_sel:WORD_1 dst_unused:UNUSED_PRESERVE src0_sel:WORD_1
	v_pk_add_f16 v42, v40, v38
	v_pk_add_f16 v43, v41, v39
	v_pk_fma_f16 v36, v38, v36, v42 neg_lo:[1,0,0] neg_hi:[1,0,0]
	v_pk_fma_f16 v37, v39, v37, v43 neg_lo:[1,0,0] neg_hi:[1,0,0]
	s_nop 0
	v_cvt_pk_f16_f32 v42, v16, v17
	v_cvt_pk_f16_f32 v43, v18, v19
	v_and_b32 v40, s35, v42
	v_and_b32 v41, s35, v43
	v_pk_fma_f16 v38, v40, s42, v227
	v_pk_fma_f16 v39, v41, s42, v227
	v_pk_fma_f16 v38, v38, v40, s43
	v_pk_fma_f16 v39, v39, v41, s43
	s_nop 0
	v_pk_mul_f16 v38, v38, v40
	v_pk_mul_f16 v39, v39, v41
	v_exp_f16_sdwa v38, v38 dst_sel:WORD_0 dst_unused:UNUSED_PRESERVE src0_sel:WORD_0
	v_exp_f16_sdwa v39, v39 dst_sel:WORD_0 dst_unused:UNUSED_PRESERVE src0_sel:WORD_0
	v_exp_f16_sdwa v38, v38 dst_sel:WORD_1 dst_unused:UNUSED_PRESERVE src0_sel:WORD_1
	v_exp_f16_sdwa v39, v39 dst_sel:WORD_1 dst_unused:UNUSED_PRESERVE src0_sel:WORD_1
	v_pk_add_f16 v16, v42, v40
	v_pk_add_f16 v17, v43, v41
	v_pk_fma_f16 v38, v40, v38, v16 neg_lo:[1,0,0] neg_hi:[1,0,0]
	v_pk_fma_f16 v39, v41, v39, v17 neg_lo:[1,0,0] neg_hi:[1,0,0]
	s_nop 0
	v_cvt_pk_f16_f32 v40, v20, v21
	v_cvt_pk_f16_f32 v41, v22, v23
	v_and_b32 v18, s35, v40
	v_and_b32 v19, s35, v41
	v_pk_fma_f16 v16, v18, s42, v227
	v_pk_fma_f16 v17, v19, s42, v227
	v_pk_fma_f16 v16, v16, v18, s43
	v_pk_fma_f16 v17, v17, v19, s43
	s_nop 0
	v_pk_mul_f16 v16, v16, v18
	v_pk_mul_f16 v17, v17, v19
	v_exp_f16_sdwa v16, v16 dst_sel:WORD_0 dst_unused:UNUSED_PRESERVE src0_sel:WORD_0
	v_exp_f16_sdwa v17, v17 dst_sel:WORD_0 dst_unused:UNUSED_PRESERVE src0_sel:WORD_0
	v_exp_f16_sdwa v16, v16 dst_sel:WORD_1 dst_unused:UNUSED_PRESERVE src0_sel:WORD_1
	v_exp_f16_sdwa v17, v17 dst_sel:WORD_1 dst_unused:UNUSED_PRESERVE src0_sel:WORD_1
	v_pk_add_f16 v20, v40, v18
	v_pk_add_f16 v21, v41, v19
	v_pk_fma_f16 v16, v18, v16, v20 neg_lo:[1,0,0] neg_hi:[1,0,0]
	v_pk_fma_f16 v17, v19, v17, v21 neg_lo:[1,0,0] neg_hi:[1,0,0]
	s_nop 0
	v_cvt_pk_f16_f32 v22, v24, v25
	v_cvt_pk_f16_f32 v23, v26, v27
	v_and_b32 v20, s35, v22
	v_and_b32 v21, s35, v23
	v_pk_fma_f16 v18, v20, s42, v227
	v_pk_fma_f16 v19, v21, s42, v227
	v_pk_fma_f16 v18, v18, v20, s43
	v_pk_fma_f16 v19, v19, v21, s43
	s_nop 0
	v_pk_mul_f16 v18, v18, v20
	v_pk_mul_f16 v19, v19, v21
	v_exp_f16_sdwa v18, v18 dst_sel:WORD_0 dst_unused:UNUSED_PRESERVE src0_sel:WORD_0
	v_exp_f16_sdwa v19, v19 dst_sel:WORD_0 dst_unused:UNUSED_PRESERVE src0_sel:WORD_0
	v_exp_f16_sdwa v18, v18 dst_sel:WORD_1 dst_unused:UNUSED_PRESERVE src0_sel:WORD_1
	v_exp_f16_sdwa v19, v19 dst_sel:WORD_1 dst_unused:UNUSED_PRESERVE src0_sel:WORD_1
	v_pk_add_f16 v24, v22, v20
	v_pk_add_f16 v25, v23, v21
	v_pk_fma_f16 v18, v20, v18, v24 neg_lo:[1,0,0] neg_hi:[1,0,0]
	v_pk_fma_f16 v19, v21, v19, v25 neg_lo:[1,0,0] neg_hi:[1,0,0]
	s_nop 0
	v_cvt_pk_f16_f32 v24, v28, v29
	v_cvt_pk_f16_f32 v25, v30, v31
	v_and_b32 v22, s35, v24
	v_and_b32 v23, s35, v25
	v_pk_fma_f16 v20, v22, s42, v227
	v_pk_fma_f16 v21, v23, s42, v227
	v_pk_fma_f16 v20, v20, v22, s43
	v_pk_fma_f16 v21, v21, v23, s43
	s_nop 0
	v_pk_mul_f16 v20, v20, v22
	v_pk_mul_f16 v21, v21, v23
	v_exp_f16_sdwa v20, v20 dst_sel:WORD_0 dst_unused:UNUSED_PRESERVE src0_sel:WORD_0
	v_exp_f16_sdwa v21, v21 dst_sel:WORD_0 dst_unused:UNUSED_PRESERVE src0_sel:WORD_0
	v_exp_f16_sdwa v20, v20 dst_sel:WORD_1 dst_unused:UNUSED_PRESERVE src0_sel:WORD_1
	v_exp_f16_sdwa v21, v21 dst_sel:WORD_1 dst_unused:UNUSED_PRESERVE src0_sel:WORD_1
	v_pk_add_f16 v26, v24, v22
	v_pk_add_f16 v27, v25, v23
	v_pk_fma_f16 v20, v22, v20, v26 neg_lo:[1,0,0] neg_hi:[1,0,0]
	v_pk_fma_f16 v21, v23, v21, v27 neg_lo:[1,0,0] neg_hi:[1,0,0]
	ds_write2st64_b64 v234, v[48:49], v[38:39] offset0:3 offset1:4
	ds_write2st64_b64 v231, v[32:33], v[16:17] offset0:7 offset1:8
	ds_write2st64_b64 v232, v[34:35], v[18:19] offset0:11 offset1:12
	ds_write2st64_b64 v233, v[36:37], v[20:21] offset0:15 offset1:16
	s_mul_i32 s0, s3, 0x280
	v_add_u32_e32 v44, s0, v248
	ds_read_b128 v[16:19], v44
	ds_read_b128 v[20:23], v44 offset:64
	s_waitcnt vmcnt(2)
	s_branch .LBB0_25

.LBB0_24:
	v_sub_f32_e32 v24, v32, v237
	v_exp_f32_e32 v24, v24
	v_sub_f32_e32 v25, v33, v237
	v_exp_f32_e32 v25, v25
	v_sub_f32_e32 v26, v34, v237
	v_exp_f32_e32 v26, v26
	v_sub_f32_e32 v27, v35, v237
	v_exp_f32_e32 v27, v27
	v_sub_f32_e32 v28, v36, v237
	v_exp_f32_e32 v28, v28
	v_sub_f32_e32 v29, v37, v237
	v_exp_f32_e32 v29, v29
	v_sub_f32_e32 v30, v38, v237
	v_exp_f32_e32 v30, v30
	v_sub_f32_e32 v31, v39, v237
	v_exp_f32_e32 v31, v31
	ds_read_b64_tr_b16 v[48:49], v251
	ds_read_b64_tr_b16 v[50:51], v251 offset:2176
	ds_read_b64_tr_b16 v[52:53], v251 offset:32
	ds_read_b64_tr_b16 v[54:55], v251 offset:2208
	ds_read_b64_tr_b16 v[56:57], v251 offset:64
	ds_read_b64_tr_b16 v[58:59], v251 offset:2240
	ds_read_b64_tr_b16 v[60:61], v251 offset:96
	ds_read_b64_tr_b16 v[62:63], v251 offset:2272
	v_cvt_pk_f16_f32 v40, v24, v25
	v_cvt_pk_f16_f32 v41, v26, v27
	v_cvt_pk_f16_f32 v42, v28, v29
	v_cvt_pk_f16_f32 v43, v30, v31
	v_dot2c_f32_f16_e32 v236, 0x3c003c00, v40
	v_dot2c_f32_f16_e32 v236, 0x3c003c00, v41
	v_dot2c_f32_f16_e32 v236, 0x3c003c00, v42
	v_dot2c_f32_f16_e32 v236, 0x3c003c00, v43
	s_waitcnt lgkmcnt(6)
	v_mfma_f32_16x16x32_f16 v[0:3], v[48:51], v[40:43], v[0:3]
	s_waitcnt lgkmcnt(4)
	v_mfma_f32_16x16x32_f16 v[4:7], v[52:55], v[40:43], v[4:7]
	s_addk_i32 s8, 0x200
	s_waitcnt lgkmcnt(2)
	v_mfma_f32_16x16x32_f16 v[8:11], v[56:59], v[40:43], v[8:11]
	s_cmpk_eq_i32 s8, 0x800
	s_waitcnt lgkmcnt(0)
	v_mfma_f32_16x16x32_f16 v[12:15], v[60:63], v[40:43], v[12:15]
	s_cbranch_scc1 .LBB0_28
.LBB0_25:
	v_mfma_f32_32x32x16_f16 v[48:63], v[80:83], v[96:99], 0
	v_add_u32_e32 v44, s8, v226
	ds_read_b128 v[32:35], v44
	ds_read_b128 v[36:39], v44 offset:4352
	v_mfma_f32_32x32x16_f16 v[64:79], v[204:207], v[96:99], 0
	s_waitcnt lgkmcnt(1)
	v_mfma_f32_32x32x16_f16 v[48:63], v[88:91], v[32:35], v[48:63]
	ds_read_b128 v[40:43], v44 offset:16
	v_mfma_f32_32x32x16_f16 v[64:79], v[84:87], v[32:35], v[64:79]
	s_waitcnt lgkmcnt(1)
	v_mfma_f32_32x32x16_f16 v[48:63], v[100:103], v[36:39], v[48:63]
	ds_read_b128 v[32:35], v44 offset:4368
	v_mfma_f32_32x32x16_f16 v[64:79], v[92:95], v[36:39], v[64:79]
	s_waitcnt lgkmcnt(1)
	v_mfma_f32_32x32x16_f16 v[48:63], v[108:111], v[40:43], v[48:63]
	ds_read_b128 v[36:39], v44 offset:32
	v_mfma_f32_32x32x16_f16 v[64:79], v[104:107], v[40:43], v[64:79]
	s_waitcnt lgkmcnt(1)
	v_mfma_f32_32x32x16_f16 v[48:63], v[116:119], v[32:35], v[48:63]
	ds_read_b128 v[40:43], v44 offset:4384
	v_mfma_f32_32x32x16_f16 v[64:79], v[112:115], v[32:35], v[64:79]
	s_waitcnt lgkmcnt(1)
	v_mfma_f32_32x32x16_f16 v[48:63], v[120:123], v[36:39], v[48:63]
	ds_read_b128 v[32:35], v44 offset:48
	v_mfma_f32_32x32x16_f16 v[64:79], v[128:131], v[36:39], v[64:79]
	s_waitcnt lgkmcnt(1)
	v_mfma_f32_32x32x16_f16 v[48:63], v[152:155], v[40:43], v[48:63]
	ds_read_b128 v[36:39], v44 offset:4400
	v_mfma_f32_32x32x16_f16 v[64:79], v[124:127], v[40:43], v[64:79]
	s_waitcnt lgkmcnt(1)
	v_mfma_f32_32x32x16_f16 v[48:63], v[136:139], v[32:35], v[48:63]
	ds_read_b128 v[40:43], v44 offset:64
	v_mfma_f32_32x32x16_f16 v[64:79], v[132:135], v[32:35], v[64:79]
	s_waitcnt lgkmcnt(1)
	v_mfma_f32_32x32x16_f16 v[48:63], v[144:147], v[36:39], v[48:63]
	ds_read_b128 v[32:35], v44 offset:4416
	v_mfma_f32_32x32x16_f16 v[64:79], v[140:143], v[36:39], v[64:79]
	s_waitcnt lgkmcnt(1)
	v_mfma_f32_32x32x16_f16 v[48:63], v[156:159], v[40:43], v[48:63]
	ds_read_b128 v[36:39], v44 offset:80
	v_mfma_f32_32x32x16_f16 v[64:79], v[148:151], v[40:43], v[64:79]
	s_waitcnt lgkmcnt(1)
	v_mfma_f32_32x32x16_f16 v[48:63], v[164:167], v[32:35], v[48:63]
	ds_read_b128 v[40:43], v44 offset:4432
	v_mfma_f32_32x32x16_f16 v[64:79], v[160:163], v[32:35], v[64:79]
	s_waitcnt lgkmcnt(1)
	v_mfma_f32_32x32x16_f16 v[48:63], v[172:175], v[36:39], v[48:63]
	ds_read_b128 v[32:35], v44 offset:96
	v_mfma_f32_32x32x16_f16 v[64:79], v[168:171], v[36:39], v[64:79]
	s_waitcnt lgkmcnt(1)
	v_mfma_f32_32x32x16_f16 v[48:63], v[180:183], v[40:43], v[48:63]
	ds_read_b128 v[36:39], v44 offset:4448
	v_mfma_f32_32x32x16_f16 v[64:79], v[176:179], v[40:43], v[64:79]
	s_waitcnt lgkmcnt(1)
	v_mfma_f32_32x32x16_f16 v[48:63], v[188:191], v[32:35], v[48:63]
	v_mfma_f32_32x32x16_f16 v[64:79], v[184:187], v[32:35], v[64:79]
	s_waitcnt lgkmcnt(0)
	v_mfma_f32_32x32x16_f16 v[48:63], v[196:199], v[36:39], v[48:63]
	v_mfma_f32_32x32x16_f16 v[64:79], v[192:195], v[36:39], v[64:79]
	s_nop 15
	s_nop 3
	v_cvt_pk_f16_f32 v38, v64, v65
	v_cvt_pk_f16_f32 v39, v66, v67
	v_and_b32 v36, s35, v38
	v_and_b32 v37, s35, v39
	v_pk_fma_f16 v238, v36, s42, v227
	v_pk_fma_f16 v239, v37, s42, v227
	v_pk_fma_f16 v238, v238, v36, s43
	v_pk_fma_f16 v239, v239, v37, s43
	s_nop 0
	v_pk_mul_f16 v238, v238, v36
	v_pk_mul_f16 v239, v239, v37
	v_exp_f16_sdwa v238, v238 dst_sel:WORD_0 dst_unused:UNUSED_PRESERVE src0_sel:WORD_0
	v_exp_f16_sdwa v239, v239 dst_sel:WORD_0 dst_unused:UNUSED_PRESERVE src0_sel:WORD_0
	v_exp_f16_sdwa v238, v238 dst_sel:WORD_1 dst_unused:UNUSED_PRESERVE src0_sel:WORD_1
	v_exp_f16_sdwa v239, v239 dst_sel:WORD_1 dst_unused:UNUSED_PRESERVE src0_sel:WORD_1
	v_pk_add_f16 v40, v38, v36
	v_pk_add_f16 v41, v39, v37
	v_pk_fma_f16 v238, v36, v238, v40 neg_lo:[1,0,0] neg_hi:[1,0,0]
	v_pk_fma_f16 v239, v37, v239, v41 neg_lo:[1,0,0] neg_hi:[1,0,0]
	v_cvt_pk_f16_f32 v38, v68, v69
	v_cvt_pk_f16_f32 v39, v70, v71
	v_and_b32 v36, s35, v38
	v_and_b32 v37, s35, v39
	v_pk_fma_f16 v240, v36, s42, v227
	v_pk_fma_f16 v241, v37, s42, v227
	v_pk_fma_f16 v240, v240, v36, s43
	v_pk_fma_f16 v241, v241, v37, s43
	v_cvt_pk_f16_f32 v243, v72, v73
	v_cvt_pk_f16_f32 v244, v74, v75
	v_and_b32 v209, s35, v243
	v_and_b32 v242, s35, v244
	v_pk_fma_f16 v68, v209, s42, v227
	v_pk_fma_f16 v69, v242, s42, v227
	v_pk_fma_f16 v68, v68, v209, s43
	v_pk_fma_f16 v69, v69, v242, s43
	v_cvt_pk_f16_f32 v74, v76, v77
	v_cvt_pk_f16_f32 v75, v78, v79
	v_and_b32 v72, s35, v74
	v_and_b32 v73, s35, v75
	v_pk_fma_f16 v70, v72, s42, v227
	v_pk_fma_f16 v71, v73, s42, v227
	v_pk_fma_f16 v70, v70, v72, s43
	v_pk_fma_f16 v71, v71, v73, s43
	s_cmp_eq_u32 s8, 0
	v_pk_mul_f16 v240, v240, v36
	v_pk_mul_f16 v241, v241, v37
	v_exp_f16_sdwa v240, v240 dst_sel:WORD_0 dst_unused:UNUSED_PRESERVE src0_sel:WORD_0
	v_exp_f16_sdwa v241, v241 dst_sel:WORD_0 dst_unused:UNUSED_PRESERVE src0_sel:WORD_0
	v_exp_f16_sdwa v240, v240 dst_sel:WORD_1 dst_unused:UNUSED_PRESERVE src0_sel:WORD_1
	v_exp_f16_sdwa v241, v241 dst_sel:WORD_1 dst_unused:UNUSED_PRESERVE src0_sel:WORD_1
	v_pk_add_f16 v40, v38, v36
	v_pk_add_f16 v41, v39, v37
	v_pk_fma_f16 v240, v36, v240, v40 neg_lo:[1,0,0] neg_hi:[1,0,0]
	v_pk_fma_f16 v241, v37, v241, v41 neg_lo:[1,0,0] neg_hi:[1,0,0]
	v_pk_mul_f16 v68, v68, v209
	v_pk_mul_f16 v69, v69, v242
	v_exp_f16_sdwa v68, v68 dst_sel:WORD_0 dst_unused:UNUSED_PRESERVE src0_sel:WORD_0
	v_exp_f16_sdwa v69, v69 dst_sel:WORD_0 dst_unused:UNUSED_PRESERVE src0_sel:WORD_0
	v_exp_f16_sdwa v68, v68 dst_sel:WORD_1 dst_unused:UNUSED_PRESERVE src0_sel:WORD_1
	v_exp_f16_sdwa v69, v69 dst_sel:WORD_1 dst_unused:UNUSED_PRESERVE src0_sel:WORD_1
	v_pk_add_f16 v76, v243, v209
	v_pk_add_f16 v77, v244, v242
	v_pk_fma_f16 v68, v209, v68, v76 neg_lo:[1,0,0] neg_hi:[1,0,0]
	v_pk_fma_f16 v69, v242, v69, v77 neg_lo:[1,0,0] neg_hi:[1,0,0]
	v_pk_mul_f16 v70, v70, v72
	v_pk_mul_f16 v71, v71, v73
	v_exp_f16_sdwa v70, v70 dst_sel:WORD_0 dst_unused:UNUSED_PRESERVE src0_sel:WORD_0
	v_exp_f16_sdwa v71, v71 dst_sel:WORD_0 dst_unused:UNUSED_PRESERVE src0_sel:WORD_0
	v_exp_f16_sdwa v70, v70 dst_sel:WORD_1 dst_unused:UNUSED_PRESERVE src0_sel:WORD_1
	v_exp_f16_sdwa v71, v71 dst_sel:WORD_1 dst_unused:UNUSED_PRESERVE src0_sel:WORD_1
	v_pk_add_f16 v76, v74, v72
	v_pk_add_f16 v77, v75, v73
	v_pk_fma_f16 v70, v72, v70, v76 neg_lo:[1,0,0] neg_hi:[1,0,0]
	v_pk_fma_f16 v71, v73, v71, v77 neg_lo:[1,0,0] neg_hi:[1,0,0]
	v_cvt_pk_f16_f32 v74, v48, v49
	v_cvt_pk_f16_f32 v75, v50, v51
	v_and_b32 v72, s35, v74
	v_and_b32 v73, s35, v75
	v_pk_fma_f16 v64, v72, s42, v227
	v_pk_fma_f16 v65, v73, s42, v227
	v_pk_fma_f16 v64, v64, v72, s43
	v_pk_fma_f16 v65, v65, v73, s43
	v_cvt_pk_f16_f32 v78, v52, v53
	v_cvt_pk_f16_f32 v79, v54, v55
	v_and_b32 v76, s35, v78
	v_and_b32 v77, s35, v79
	v_pk_fma_f16 v66, v76, s42, v227
	v_pk_fma_f16 v67, v77, s42, v227
	v_pk_fma_f16 v66, v66, v76, s43
	v_pk_fma_f16 v67, v67, v77, s43
	v_pk_mul_f16 v64, v64, v72
	v_pk_mul_f16 v65, v65, v73
	v_exp_f16_sdwa v64, v64 dst_sel:WORD_0 dst_unused:UNUSED_PRESERVE src0_sel:WORD_0
	v_exp_f16_sdwa v65, v65 dst_sel:WORD_0 dst_unused:UNUSED_PRESERVE src0_sel:WORD_0
	v_exp_f16_sdwa v64, v64 dst_sel:WORD_1 dst_unused:UNUSED_PRESERVE src0_sel:WORD_1
	v_exp_f16_sdwa v65, v65 dst_sel:WORD_1 dst_unused:UNUSED_PRESERVE src0_sel:WORD_1
	v_pk_add_f16 v209, v74, v72
	v_pk_add_f16 v242, v75, v73
	v_pk_fma_f16 v64, v72, v64, v209 neg_lo:[1,0,0] neg_hi:[1,0,0]
	v_pk_fma_f16 v65, v73, v65, v242 neg_lo:[1,0,0] neg_hi:[1,0,0]
	v_pk_mul_f16 v66, v66, v76
	v_pk_mul_f16 v67, v67, v77
	v_exp_f16_sdwa v66, v66 dst_sel:WORD_0 dst_unused:UNUSED_PRESERVE src0_sel:WORD_0
	v_exp_f16_sdwa v67, v67 dst_sel:WORD_0 dst_unused:UNUSED_PRESERVE src0_sel:WORD_0
	v_exp_f16_sdwa v66, v66 dst_sel:WORD_1 dst_unused:UNUSED_PRESERVE src0_sel:WORD_1
	v_exp_f16_sdwa v67, v67 dst_sel:WORD_1 dst_unused:UNUSED_PRESERVE src0_sel:WORD_1
	v_pk_add_f16 v72, v78, v76
	v_pk_add_f16 v73, v79, v77
	v_pk_fma_f16 v66, v76, v66, v72 neg_lo:[1,0,0] neg_hi:[1,0,0]
	v_pk_fma_f16 v67, v77, v67, v73 neg_lo:[1,0,0] neg_hi:[1,0,0]
	v_cvt_pk_f16_f32 v74, v56, v57
	v_cvt_pk_f16_f32 v75, v58, v59
	v_and_b32 v72, s35, v74
	v_and_b32 v73, s35, v75
	v_pk_fma_f16 v48, v72, s42, v227
	v_pk_fma_f16 v49, v73, s42, v227
	v_pk_fma_f16 v48, v48, v72, s43
	v_pk_fma_f16 v49, v49, v73, s43
	v_cvt_pk_f16_f32 v58, v60, v61
	v_cvt_pk_f16_f32 v59, v62, v63
	v_and_b32 v56, s35, v58
	v_and_b32 v57, s35, v59
	v_pk_fma_f16 v50, v56, s42, v227
	v_pk_fma_f16 v51, v57, s42, v227
	v_pk_fma_f16 v50, v50, v56, s43
	v_pk_fma_f16 v51, v51, v57, s43
	v_pk_mul_f16 v48, v48, v72
	v_pk_mul_f16 v49, v49, v73
	v_exp_f16_sdwa v48, v48 dst_sel:WORD_0 dst_unused:UNUSED_PRESERVE src0_sel:WORD_0
	v_exp_f16_sdwa v49, v49 dst_sel:WORD_0 dst_unused:UNUSED_PRESERVE src0_sel:WORD_0
	v_exp_f16_sdwa v48, v48 dst_sel:WORD_1 dst_unused:UNUSED_PRESERVE src0_sel:WORD_1
	v_exp_f16_sdwa v49, v49 dst_sel:WORD_1 dst_unused:UNUSED_PRESERVE src0_sel:WORD_1
	v_pk_add_f16 v62, v74, v72
	v_pk_add_f16 v63, v75, v73
	v_pk_fma_f16 v48, v72, v48, v62 neg_lo:[1,0,0] neg_hi:[1,0,0]
	v_pk_fma_f16 v49, v73, v49, v63 neg_lo:[1,0,0] neg_hi:[1,0,0]
	v_pk_mul_f16 v50, v50, v56
	v_pk_mul_f16 v51, v51, v57
	v_exp_f16_sdwa v50, v50 dst_sel:WORD_0 dst_unused:UNUSED_PRESERVE src0_sel:WORD_0
	v_exp_f16_sdwa v51, v51 dst_sel:WORD_0 dst_unused:UNUSED_PRESERVE src0_sel:WORD_0
	v_exp_f16_sdwa v50, v50 dst_sel:WORD_1 dst_unused:UNUSED_PRESERVE src0_sel:WORD_1
	v_exp_f16_sdwa v51, v51 dst_sel:WORD_1 dst_unused:UNUSED_PRESERVE src0_sel:WORD_1
	v_pk_add_f16 v62, v58, v56
	v_pk_add_f16 v63, v59, v57
	v_pk_fma_f16 v50, v56, v50, v62 neg_lo:[1,0,0] neg_hi:[1,0,0]
	v_pk_fma_f16 v51, v57, v51, v63 neg_lo:[1,0,0] neg_hi:[1,0,0]
	ds_write2_b64 v246, v[238:239], v[240:241] offset0:136 offset1:138
	ds_write2_b64 v246, v[64:65], v[66:67] offset0:144 offset1:146
	ds_write2_b64 v246, v[68:69], v[70:71] offset0:140 offset1:142
	ds_write2_b64 v246, v[48:49], v[50:51] offset0:148 offset1:150
	ds_read2_b64 v[24:27], v249 offset1:1
	ds_read2_b64 v[28:31], v249 offset0:8 offset1:9
	ds_read2_b64 v[40:43], v250 offset1:1
	ds_read2_b64 v[44:47], v250 offset0:8 offset1:9
	s_waitcnt lgkmcnt(2)
	v_mfma_f32_16x16x32_f16 v[32:35], v[24:27], v[16:19], 0
	v_mfma_f32_16x16x32_f16 v[32:35], v[28:31], v[20:23], v[32:35]
	s_waitcnt lgkmcnt(0)
	v_mfma_f32_16x16x32_f16 v[36:39], v[40:43], v[16:19], 0
	v_mfma_f32_16x16x32_f16 v[36:39], v[44:47], v[20:23], v[36:39]
	s_nop 7
	v_max3_f32 v52, v32, v33, v34
	v_max3_f32 v52, v52, v35, v36
	v_max3_f32 v52, v52, v37, v38
	v_max_f32_e32 v52, v52, v39
	ds_bpermute_b32 v53, v247, v52
	s_waitcnt lgkmcnt(0)
	v_max_f32_e32 v52, v52, v53
	ds_bpermute_b32 v53, v245, v52
	s_waitcnt lgkmcnt(0)
	v_max_f32_e32 v48, v52, v53
	s_cbranch_scc1 .LBB0_23
	v_add_f32_e32 v49, 0x41000000, v237
	v_cmp_gt_f32_e32 vcc, v48, v49
	s_cbranch_vccz .LBB0_24
	v_max_f32_e32 v48, v48, v48
	v_max_f32_e32 v49, v237, v237
	v_max_f32_e32 v49, v49, v48
	v_sub_f32_e32 v48, v237, v49
	v_exp_f32_e32 v48, v48
	v_mov_b32_e32 v237, v49
	v_pk_mul_f32 v[14:15], v[48:49], v[14:15] op_sel_hi:[0,1]
	v_pk_mul_f32 v[12:13], v[48:49], v[12:13] op_sel_hi:[0,1]
	v_pk_mul_f32 v[10:11], v[48:49], v[10:11] op_sel_hi:[0,1]
	v_pk_mul_f32 v[8:9], v[48:49], v[8:9] op_sel_hi:[0,1]
	v_pk_mul_f32 v[6:7], v[48:49], v[6:7] op_sel_hi:[0,1]
	v_pk_mul_f32 v[4:5], v[48:49], v[4:5] op_sel_hi:[0,1]
	v_pk_mul_f32 v[2:3], v[48:49], v[2:3] op_sel_hi:[0,1]
	v_pk_mul_f32 v[0:1], v[48:49], v[0:1] op_sel_hi:[0,1]
	v_mul_f32_e32 v236, v236, v48
	s_branch .LBB0_24
.LBB0_28:
	ds_bpermute_b32 v32, v247, v236
	v_and_b32_e32 v40, 15, v215
	s_waitcnt lgkmcnt(0)
	v_add_f32_e32 v41, v236, v32
	s_nop 0
	ds_bpermute_b32 v32, v245, v41
	v_cmp_gt_u32_e32 vcc, 5, v40
	s_nop 1
	s_and_saveexec_b64 s[0:1], vcc
	s_cbranch_execz .LBB0_21
	s_waitcnt lgkmcnt(0)
	v_add_f32_e32 v32, v41, v32
	v_div_scale_f32 v33, s[10:11], v32, v32, 0.5
	v_rcp_f32_e32 v34, v33
	v_div_scale_f32 v35, vcc, 0.5, v32, 0.5
	v_fma_f32 v36, -v33, v34, 1.0
	v_fmac_f32_e32 v34, v36, v34
	v_mul_f32_e32 v36, v35, v34
	v_fma_f32 v37, -v33, v36, v35
	v_fmac_f32_e32 v36, v37, v34
	v_fma_f32 v33, -v33, v36, v35
	v_div_fmas_f32 v33, v33, v34, v36
	v_div_fixup_f32 v32, v33, v32, 0.5
	v_add_u32_e32 v33, s3, v221
	v_mov_b32_e32 v34, v40
	v_mad_u64_u32 v[34:35], s[8:9], v33, 5, v[34:35]
	v_lshl_add_u32 v33, v34, 7, v252
	v_pk_mul_f32 v[44:45], v[32:33], v[0:1] op_sel_hi:[0,1]
	v_pk_mul_f32 v[46:47], v[32:33], v[2:3] op_sel_hi:[0,1]
	v_cvt_pk_f16_f32 v44, v44, v45
	v_cvt_pk_f16_f32 v45, v46, v47
	ds_write_b64 v33, v[44:45]
	v_pk_mul_f32 v[48:49], v[32:33], v[4:5] op_sel_hi:[0,1]
	v_pk_mul_f32 v[50:51], v[32:33], v[6:7] op_sel_hi:[0,1]
	v_cvt_pk_f16_f32 v48, v48, v49
	v_cvt_pk_f16_f32 v49, v50, v51
	ds_write_b64 v33, v[48:49] offset:32
	v_pk_mul_f32 v[52:53], v[32:33], v[8:9] op_sel_hi:[0,1]
	v_pk_mul_f32 v[54:55], v[32:33], v[10:11] op_sel_hi:[0,1]
	v_cvt_pk_f16_f32 v52, v52, v53
	v_cvt_pk_f16_f32 v53, v54, v55
	ds_write_b64 v33, v[52:53] offset:64
	v_pk_mul_f32 v[56:57], v[32:33], v[12:13] op_sel_hi:[0,1]
	v_pk_mul_f32 v[58:59], v[32:33], v[14:15] op_sel_hi:[0,1]
	v_cvt_pk_f16_f32 v56, v56, v57
	v_cvt_pk_f16_f32 v57, v58, v59
	ds_write_b64 v33, v[56:57] offset:96
	s_branch .LBB0_21
